# speedup vs baseline: 1.0613x; 1.0039x over previous
.LBB2_2:
	v_lshl_add_u64 v[38:39], v[102:103], 0, s[6:7]
	v_lshl_add_u64 v[40:41], v[100:101], 0, s[6:7]
	global_load_dwordx4 v[94:97], v[38:39], off
	global_load_dwordx4 v[90:93], v[38:39], off offset:1024
	global_load_dwordx4 v[86:89], v[38:39], off offset:2048
	global_load_dwordx4 v[82:85], v[38:39], off offset:3072
	v_add_co_u32_e32 v38, vcc, s8, v40
	s_waitcnt vmcnt(4)
	v_mov_b64_e32 v[34:35], v[78:79]
	v_mov_b64_e32 v[108:109], v[76:77]
	v_mov_b64_e32 v[112:113], v[72:73]
	v_mov_b64_e32 v[116:117], v[68:69]
	v_addc_co_u32_e32 v39, vcc, 0, v41, vcc
	v_mov_b64_e32 v[36:37], v[80:81]
	v_mov_b64_e32 v[106:107], v[74:75]
	v_mov_b64_e32 v[110:111], v[70:71]
	v_mov_b64_e32 v[114:115], v[66:67]
	global_load_dwordx4 v[78:81], v[38:39], off
	global_load_dwordx4 v[74:77], v[38:39], off offset:1024
	global_load_dwordx4 v[70:73], v[38:39], off offset:2048
	global_load_dwordx4 v[66:69], v[38:39], off offset:3072
	v_mov_b32_e32 v105, v131
	v_mov_b32_e32 v118, v104
	s_setprio 1
	v_mfma_f32_32x32x16_f16 v[34:49], v[34:37], v[62:65], 0
	v_mfma_f32_32x32x16_f16 v[34:49], v[106:109], v[58:61], v[34:49]
	v_mfma_f32_32x32x16_f16 v[34:49], v[110:113], v[54:57], v[34:49]
	v_mfma_f32_32x32x16_f16 v[34:49], v[114:117], v[50:53], v[34:49]
	s_setprio 0
	s_nop 10
	v_max_f32_e32 v104, v35, v35
	v_max_f32_e32 v106, v34, v34
	v_max_f32_e32 v104, v106, v104
	v_max3_f32 v104, v104, v36, v37
	v_max3_f32 v104, v104, v38, v39
	v_max3_f32 v104, v104, v40, v41
	v_max3_f32 v104, v104, v42, v43
	v_max3_f32 v104, v104, v44, v45
	v_max3_f32 v104, v104, v46, v47
	v_max3_f32 v104, v104, v48, v49
	ds_bpermute_b32 v106, v138, v104
	s_waitcnt lgkmcnt(0)
	v_max3_f32 v104, v118, v104, v106
	v_sub_f32_e32 v34, v34, v104
	v_sub_f32_e32 v35, v35, v104
	v_exp_f32_e32 v107, v34
	v_exp_f32_e32 v108, v35
	v_sub_f32_e32 v36, v36, v104
	v_sub_f32_e32 v34, v37, v104
	v_exp_f32_e32 v35, v36
	v_add_f32_e32 v36, 0, v107
	v_exp_f32_e32 v109, v34
	v_sub_f32_e32 v34, v38, v104
	v_exp_f32_e32 v38, v34
	v_add_f32_e32 v34, v108, v36
	v_sub_f32_e32 v36, v39, v104
	v_exp_f32_e32 v36, v36
	v_sub_f32_e32 v37, v40, v104
	v_add_f32_e32 v34, v35, v34
	v_exp_f32_e32 v37, v37
	v_sub_f32_e32 v39, v41, v104
	v_add_f32_e32 v34, v109, v34
	v_exp_f32_e32 v39, v39
	v_sub_f32_e32 v40, v42, v104
	v_add_f32_e32 v34, v38, v34
	v_exp_f32_e32 v42, v40
	v_sub_f32_e32 v40, v43, v104
	v_add_f32_e32 v34, v36, v34
	v_exp_f32_e32 v43, v40
	v_sub_f32_e32 v40, v44, v104
	v_add_f32_e32 v34, v37, v34
	v_exp_f32_e32 v44, v40
	v_sub_f32_e32 v40, v45, v104
	v_add_f32_e32 v34, v39, v34
	v_exp_f32_e32 v45, v40
	v_sub_f32_e32 v40, v46, v104
	v_add_f32_e32 v34, v42, v34
	v_exp_f32_e32 v40, v40
	v_add_f32_e32 v34, v43, v34
	v_add_f32_e32 v34, v44, v34
	v_add_f32_e32 v34, v45, v34
	v_add_f32_e32 v41, v40, v34
	v_sub_f32_e32 v34, v47, v104
	v_exp_f32_e32 v46, v34
	v_sub_f32_e32 v34, v48, v104
	v_exp_f32_e32 v47, v34
	v_sub_f32_e32 v34, v49, v104
	v_sub_f32_e32 v106, v118, v104
	v_exp_f32_e32 v48, v34
	v_exp_f32_e32 v34, v106
	v_add_f32_e32 v41, v46, v41
	v_add_f32_e32 v41, v47, v41
	v_add_f32_e32 v131, v48, v41
	v_fmac_f32_e32 v131, v105, v34
	v_mul_f32_e32 v32, v34, v32
	v_mul_f32_e32 v33, v34, v33
	v_mul_f32_e32 v30, v34, v30
	v_mul_f32_e32 v31, v34, v31
	v_mul_f32_e32 v28, v34, v28
	v_mul_f32_e32 v29, v34, v29
	v_mul_f32_e32 v26, v34, v26
	v_mul_f32_e32 v27, v34, v27
	v_mul_f32_e32 v24, v34, v24
	v_mul_f32_e32 v25, v34, v25
	v_mul_f32_e32 v22, v34, v22
	v_mul_f32_e32 v23, v34, v23
	v_mul_f32_e32 v20, v34, v20
	v_mul_f32_e32 v21, v34, v21
	v_mul_f32_e32 v18, v34, v18
	v_mul_f32_e32 v19, v34, v19
	v_mul_f32_e32 v16, v34, v16
	v_mul_f32_e32 v17, v34, v17
	v_mul_f32_e32 v14, v34, v14
	v_mul_f32_e32 v15, v34, v15
	v_mul_f32_e32 v12, v34, v12
	v_mul_f32_e32 v13, v34, v13
	v_mul_f32_e32 v10, v34, v10
	v_mul_f32_e32 v11, v34, v11
	v_mul_f32_e32 v8, v34, v8
	v_mul_f32_e32 v9, v34, v9
	v_mul_f32_e32 v6, v34, v6
	v_mul_f32_e32 v7, v34, v7
	v_mul_f32_e32 v4, v34, v4
	v_mul_f32_e32 v5, v34, v5
	v_mul_f32_e32 v2, v34, v2
	v_mul_f32_e32 v3, v34, v3
	v_cvt_pk_f16_f32 v37, v37, v39
	v_cvt_pk_f16_f32 v36, v38, v36
	v_cvt_pk_f16_f32 v35, v35, v109
	v_cvt_pk_f16_f32 v34, v107, v108
	v_cvt_pk_f16_f32 v41, v47, v48
	v_cvt_pk_f16_f32 v40, v40, v46
	v_cvt_pk_f16_f32 v39, v44, v45
	v_cvt_pk_f16_f32 v38, v42, v43
	s_setprio 1
	s_waitcnt vmcnt(7)
	v_mfma_f32_32x32x16_f16 v[18:33], v[94:97], v[34:37], v[18:33]
	s_waitcnt vmcnt(5)
	v_mfma_f32_32x32x16_f16 v[2:17], v[86:89], v[34:37], v[2:17]
	v_mfma_f32_32x32x16_f16 v[18:33], v[90:93], v[38:41], v[18:33]
	s_waitcnt vmcnt(4)
	v_mfma_f32_32x32x16_f16 v[2:17], v[82:85], v[38:41], v[2:17]
	s_setprio 0
	s_add_u32 s6, s6, 0x1000
	s_addc_u32 s7, s7, 0
	s_cmpk_lg_i32 s6, 0x3000
	s_cbranch_scc1 .LBB2_2
	v_lshl_add_u64 v[34:35], v[98:99], 4, s[50:51]
	v_mov_b32_e32 v37, 0
	v_mov_b32_e32 v36, v130
	v_lshl_add_u64 v[34:35], v[34:35], 0, v[36:37]
	v_add_co_u32_e32 v34, vcc, 0x3000, v34
	s_nop 1
	v_addc_co_u32_e32 v35, vcc, 0, v35, vcc
	global_load_dwordx4 v[82:85], v[34:35], off offset:3072
	global_load_dwordx4 v[86:89], v[34:35], off offset:2048
	global_load_dwordx4 v[90:93], v[34:35], off offset:1024
	global_load_dwordx4 v[94:97], v[34:35], off
	s_setprio 1
	s_waitcnt vmcnt(7)
	v_mfma_f32_32x32x16_f16 v[34:49], v[78:81], v[62:65], 0
	s_waitcnt vmcnt(6)
	v_mfma_f32_32x32x16_f16 v[34:49], v[74:77], v[58:61], v[34:49]
	s_waitcnt vmcnt(5)
	v_mfma_f32_32x32x16_f16 v[34:49], v[70:73], v[54:57], v[34:49]
	s_waitcnt vmcnt(4)
	v_mfma_f32_32x32x16_f16 v[34:49], v[66:69], v[50:53], v[34:49]
	s_setprio 0
	s_nop 10
	v_max_f32_e32 v50, v35, v35
	v_max_f32_e32 v51, v34, v34
	v_max_f32_e32 v50, v51, v50
	v_max3_f32 v50, v50, v36, v37
	v_max3_f32 v50, v50, v38, v39
	v_max3_f32 v50, v50, v40, v41
	v_max3_f32 v50, v50, v42, v43
	v_max3_f32 v50, v50, v44, v45
	v_max3_f32 v50, v50, v46, v47
	v_max3_f32 v50, v50, v48, v49
	ds_bpermute_b32 v51, v138, v50
	s_waitcnt lgkmcnt(0)
	v_max3_f32 v135, v104, v50, v51
	v_sub_f32_e32 v34, v34, v135
	v_sub_f32_e32 v35, v35, v135
	v_exp_f32_e32 v51, v34
	v_exp_f32_e32 v52, v35
	v_sub_f32_e32 v36, v36, v135
	v_sub_f32_e32 v34, v37, v135
	v_exp_f32_e32 v35, v36
	v_add_f32_e32 v36, 0, v51
	v_exp_f32_e32 v53, v34
	v_sub_f32_e32 v34, v38, v135
	v_exp_f32_e32 v38, v34
	v_add_f32_e32 v34, v52, v36
	v_sub_f32_e32 v36, v39, v135
	v_exp_f32_e32 v36, v36
	v_sub_f32_e32 v37, v40, v135
	v_add_f32_e32 v34, v35, v34
	v_exp_f32_e32 v37, v37
	v_sub_f32_e32 v39, v41, v135
	v_add_f32_e32 v34, v53, v34
	v_exp_f32_e32 v39, v39
	v_sub_f32_e32 v40, v42, v135
	v_add_f32_e32 v34, v38, v34
	v_exp_f32_e32 v42, v40
	v_sub_f32_e32 v40, v43, v135
	v_add_f32_e32 v34, v36, v34
	v_exp_f32_e32 v43, v40
	v_sub_f32_e32 v40, v44, v135
	v_add_f32_e32 v34, v37, v34
	v_exp_f32_e32 v44, v40
	v_sub_f32_e32 v40, v45, v135
	v_add_f32_e32 v34, v39, v34
	v_exp_f32_e32 v45, v40
	v_sub_f32_e32 v40, v46, v135
	v_add_f32_e32 v34, v42, v34
	v_exp_f32_e32 v40, v40
	v_add_f32_e32 v34, v43, v34
	v_add_f32_e32 v34, v44, v34
	v_add_f32_e32 v34, v45, v34
	v_add_f32_e32 v41, v40, v34
	v_sub_f32_e32 v34, v47, v135
	v_exp_f32_e32 v46, v34
	v_sub_f32_e32 v34, v48, v135
	v_exp_f32_e32 v47, v34
	v_sub_f32_e32 v34, v49, v135
	v_sub_f32_e32 v50, v104, v135
	v_exp_f32_e32 v48, v34
	v_exp_f32_e32 v34, v50
	v_add_f32_e32 v41, v46, v41
	v_add_f32_e32 v41, v47, v41
	v_add_f32_e32 v134, v48, v41
	v_fmac_f32_e32 v134, v131, v34
	v_mul_f32_e32 v32, v34, v32
	v_mul_f32_e32 v33, v34, v33
	v_mul_f32_e32 v30, v34, v30
	v_mul_f32_e32 v31, v34, v31
	v_mul_f32_e32 v28, v34, v28
	v_mul_f32_e32 v29, v34, v29
	v_mul_f32_e32 v26, v34, v26
	v_mul_f32_e32 v27, v34, v27
	v_mul_f32_e32 v24, v34, v24
	v_mul_f32_e32 v25, v34, v25
	v_mul_f32_e32 v22, v34, v22
	v_mul_f32_e32 v23, v34, v23
	v_mul_f32_e32 v20, v34, v20
	v_mul_f32_e32 v21, v34, v21
	v_mul_f32_e32 v18, v34, v18
	v_mul_f32_e32 v19, v34, v19
	v_mul_f32_e32 v16, v34, v16
	v_mul_f32_e32 v17, v34, v17
	v_mul_f32_e32 v14, v34, v14
	v_mul_f32_e32 v15, v34, v15
	v_mul_f32_e32 v12, v34, v12
	v_mul_f32_e32 v13, v34, v13
	v_mul_f32_e32 v10, v34, v10
	v_mul_f32_e32 v11, v34, v11
	v_mul_f32_e32 v8, v34, v8
	v_mul_f32_e32 v9, v34, v9
	v_mul_f32_e32 v6, v34, v6
	v_mul_f32_e32 v7, v34, v7
	v_mul_f32_e32 v4, v34, v4
	v_mul_f32_e32 v5, v34, v5
	v_mul_f32_e32 v2, v34, v2
	v_mul_f32_e32 v3, v34, v3
	v_cvt_pk_f16_f32 v37, v37, v39
	v_cvt_pk_f16_f32 v36, v38, v36
	v_cvt_pk_f16_f32 v35, v35, v53
	v_cvt_pk_f16_f32 v34, v51, v52
	v_cvt_pk_f16_f32 v41, v47, v48
	v_cvt_pk_f16_f32 v40, v40, v46
	v_cvt_pk_f16_f32 v39, v44, v45
	v_cvt_pk_f16_f32 v38, v42, v43
	s_setprio 1
	s_waitcnt vmcnt(0)
	v_mfma_f32_32x32x16_f16 v[18:33], v[94:97], v[34:37], v[18:33]
	v_mfma_f32_32x32x16_f16 v[2:17], v[86:89], v[34:37], v[2:17]
	v_mfma_f32_32x32x16_f16 v[18:33], v[90:93], v[38:41], v[18:33]
	v_mfma_f32_32x32x16_f16 v[2:17], v[82:85], v[38:41], v[2:17]
	s_setprio 0

.LBB2_10:
	s_nop 8
	v_max_f32_e32 v98, v35, v35
	v_max_f32_e32 v99, v34, v34
	v_max_f32_e32 v98, v99, v98
	v_max3_f32 v98, v98, v36, v37
	v_max3_f32 v98, v98, v38, v39
	v_max3_f32 v98, v98, v40, v41
	v_max3_f32 v98, v98, v42, v43
	v_max3_f32 v98, v98, v44, v45
	v_max3_f32 v98, v98, v46, v47
	v_max3_f32 v98, v98, v48, v49
	ds_bpermute_b32 v99, v138, v98
	s_waitcnt lgkmcnt(0)
	v_max3_f32 v98, v119, v98, v99
	v_sub_f32_e32 v34, v34, v98
	v_sub_f32_e32 v35, v35, v98
	v_exp_f32_e32 v100, v34
	v_exp_f32_e32 v35, v35
	v_sub_f32_e32 v36, v36, v98
	v_sub_f32_e32 v34, v37, v98
	v_exp_f32_e32 v37, v36
	v_add_f32_e32 v36, 0, v100
	v_exp_f32_e32 v101, v34
	v_sub_f32_e32 v34, v38, v98
	v_exp_f32_e32 v38, v34
	v_add_f32_e32 v34, v35, v36
	v_sub_f32_e32 v36, v39, v98
	v_exp_f32_e32 v102, v36
	v_sub_f32_e32 v36, v40, v98
	v_add_f32_e32 v34, v37, v34
	v_exp_f32_e32 v39, v36
	v_sub_f32_e32 v36, v41, v98
	v_add_f32_e32 v34, v101, v34
	v_exp_f32_e32 v40, v36
	v_sub_f32_e32 v36, v42, v98
	v_add_f32_e32 v34, v38, v34
	v_exp_f32_e32 v103, v36
	v_sub_f32_e32 v36, v43, v98
	v_add_f32_e32 v34, v102, v34
	v_exp_f32_e32 v104, v36
	v_sub_f32_e32 v36, v44, v98
	v_add_f32_e32 v34, v39, v34
	v_exp_f32_e32 v41, v36
	v_sub_f32_e32 v36, v45, v98
	v_add_f32_e32 v34, v40, v34
	v_exp_f32_e32 v44, v36
	v_sub_f32_e32 v36, v46, v98
	v_add_f32_e32 v34, v103, v34
	v_exp_f32_e32 v42, v36
	v_sub_f32_e32 v36, v47, v98
	v_add_f32_e32 v34, v104, v34
	v_exp_f32_e32 v45, v36
	v_sub_f32_e32 v36, v48, v98
	v_add_f32_e32 v34, v41, v34
	v_exp_f32_e32 v43, v36
	v_sub_f32_e32 v36, v49, v98
	v_sub_f32_e32 v99, v119, v98
	v_add_f32_e32 v34, v44, v34
	v_exp_f32_e32 v46, v36
	v_add_f32_e32 v34, v42, v34
	v_exp_f32_e32 v36, v99
	v_add_f32_e32 v34, v45, v34
	v_add_f32_e32 v34, v43, v34
	v_add_f32_e32 v34, v46, v34
	v_fmac_f32_e32 v34, v131, v36
	v_mul_f32_e32 v32, v36, v32
	v_mul_f32_e32 v33, v36, v33
	v_mul_f32_e32 v30, v36, v30
	v_mul_f32_e32 v31, v36, v31
	v_mul_f32_e32 v28, v36, v28
	v_mul_f32_e32 v29, v36, v29
	v_mul_f32_e32 v26, v36, v26
	v_mul_f32_e32 v27, v36, v27
	v_mul_f32_e32 v24, v36, v24
	v_mul_f32_e32 v25, v36, v25
	v_mul_f32_e32 v22, v36, v22
	v_mul_f32_e32 v23, v36, v23
	v_mul_f32_e32 v20, v36, v20
	v_mul_f32_e32 v21, v36, v21
	v_mul_f32_e32 v18, v36, v18
	v_mul_f32_e32 v19, v36, v19
	v_mul_f32_e32 v16, v36, v16
	v_mul_f32_e32 v17, v36, v17
	v_mul_f32_e32 v14, v36, v14
	v_mul_f32_e32 v15, v36, v15
	v_mul_f32_e32 v12, v36, v12
	v_mul_f32_e32 v13, v36, v13
	v_mul_f32_e32 v10, v36, v10
	v_mul_f32_e32 v11, v36, v11
	v_mul_f32_e32 v8, v36, v8
	v_mul_f32_e32 v9, v36, v9
	v_mul_f32_e32 v6, v36, v6
	v_mul_f32_e32 v7, v36, v7
	v_mul_f32_e32 v4, v36, v4
	v_mul_f32_e32 v5, v36, v5
	v_mul_f32_e32 v2, v36, v2
	v_mul_f32_e32 v3, v36, v3
	v_cvt_pk_f16_f32 v39, v39, v40
	v_cvt_pk_f16_f32 v38, v38, v102
	v_cvt_pk_f16_f32 v37, v37, v101
	v_cvt_pk_f16_f32 v36, v100, v35
	v_cvt_pk_f16_f32 v43, v43, v46
	v_cvt_pk_f16_f32 v42, v42, v45
	v_cvt_pk_f16_f32 v41, v41, v44
	v_cvt_pk_f16_f32 v40, v103, v104
	s_setprio 1
	s_waitcnt vmcnt(3)
	v_mfma_f32_32x32x16_f16 v[18:33], v[94:97], v[36:39], v[18:33]
	s_waitcnt vmcnt(1)
	v_mfma_f32_32x32x16_f16 v[2:17], v[86:89], v[36:39], v[2:17]
	v_mfma_f32_32x32x16_f16 v[18:33], v[90:93], v[40:43], v[18:33]
	s_waitcnt vmcnt(0)
	v_mfma_f32_32x32x16_f16 v[2:17], v[82:85], v[40:43], v[2:17]
	s_setprio 0
	s_add_i32 s55, s55, 1
	s_add_u32 s2, s2, 0x1000
	s_addc_u32 s3, s3, 0
	s_cmp_lg_u32 s46, s2
	s_cbranch_scc0 .LBB2_12
	v_mov_b32_e32 v119, v98
	v_mov_b32_e32 v131, v34
	v_mov_b64_e32 v[100:101], v[68:69]
	v_mov_b64_e32 v[104:105], v[72:73]
	v_mov_b64_e32 v[108:109], v[76:77]
	v_mov_b64_e32 v[34:35], v[78:79]
	v_mov_b64_e32 v[98:99], v[66:67]
	v_mov_b64_e32 v[102:103], v[70:71]
	v_mov_b64_e32 v[106:107], v[74:75]
	v_mov_b64_e32 v[36:37], v[80:81]
	s_branch .LBB2_6

.LBB2_17:
	s_nop 8
	v_max_f32_e32 v98, v35, v35
	v_max_f32_e32 v99, v34, v34
	v_max_f32_e32 v98, v99, v98
	v_max3_f32 v98, v98, v36, v37
	v_max3_f32 v98, v98, v38, v39
	v_max3_f32 v98, v98, v40, v41
	v_max3_f32 v98, v98, v42, v43
	v_max3_f32 v98, v98, v44, v45
	v_max3_f32 v98, v98, v46, v47
	v_max3_f32 v98, v98, v48, v49
	ds_bpermute_b32 v99, v138, v98
	s_waitcnt lgkmcnt(0)
	v_max3_f32 v135, v115, v98, v99
	v_sub_f32_e32 v34, v34, v135
	v_sub_f32_e32 v35, v35, v135
	v_exp_f32_e32 v99, v34
	v_exp_f32_e32 v100, v35
	v_sub_f32_e32 v36, v36, v135
	v_sub_f32_e32 v34, v37, v135
	v_exp_f32_e32 v35, v36
	v_add_f32_e32 v36, 0, v99
	v_exp_f32_e32 v101, v34
	v_sub_f32_e32 v34, v38, v135
	v_exp_f32_e32 v38, v34
	v_add_f32_e32 v34, v100, v36
	v_sub_f32_e32 v36, v39, v135
	v_exp_f32_e32 v36, v36
	v_sub_f32_e32 v37, v40, v135
	v_add_f32_e32 v34, v35, v34
	v_exp_f32_e32 v37, v37
	v_sub_f32_e32 v39, v41, v135
	v_add_f32_e32 v34, v101, v34
	v_exp_f32_e32 v39, v39
	v_sub_f32_e32 v40, v42, v135
	v_add_f32_e32 v34, v38, v34
	v_exp_f32_e32 v42, v40
	v_sub_f32_e32 v40, v43, v135
	v_add_f32_e32 v34, v36, v34
	v_exp_f32_e32 v43, v40
	v_sub_f32_e32 v40, v44, v135
	v_add_f32_e32 v34, v37, v34
	v_exp_f32_e32 v44, v40
	v_sub_f32_e32 v40, v45, v135
	v_add_f32_e32 v34, v39, v34
	v_exp_f32_e32 v45, v40
	v_sub_f32_e32 v40, v46, v135
	v_add_f32_e32 v34, v42, v34
	v_exp_f32_e32 v40, v40
	v_add_f32_e32 v34, v43, v34
	v_add_f32_e32 v34, v44, v34
	v_add_f32_e32 v34, v45, v34
	v_add_f32_e32 v41, v40, v34
	v_sub_f32_e32 v34, v47, v135
	v_exp_f32_e32 v46, v34
	v_sub_f32_e32 v34, v48, v135
	v_exp_f32_e32 v47, v34
	v_sub_f32_e32 v34, v49, v135
	v_sub_f32_e32 v98, v115, v135
	v_exp_f32_e32 v48, v34
	v_exp_f32_e32 v34, v98
	v_add_f32_e32 v41, v46, v41
	v_add_f32_e32 v41, v47, v41
	v_add_f32_e32 v134, v48, v41
	v_fmac_f32_e32 v134, v131, v34
	v_mul_f32_e32 v32, v34, v32
	v_mul_f32_e32 v33, v34, v33
	v_mul_f32_e32 v30, v34, v30
	v_mul_f32_e32 v31, v34, v31
	v_mul_f32_e32 v28, v34, v28
	v_mul_f32_e32 v29, v34, v29
	v_mul_f32_e32 v26, v34, v26
	v_mul_f32_e32 v27, v34, v27
	v_mul_f32_e32 v24, v34, v24
	v_mul_f32_e32 v25, v34, v25
	v_mul_f32_e32 v22, v34, v22
	v_mul_f32_e32 v23, v34, v23
	v_mul_f32_e32 v20, v34, v20
	v_mul_f32_e32 v21, v34, v21
	v_mul_f32_e32 v18, v34, v18
	v_mul_f32_e32 v19, v34, v19
	v_mul_f32_e32 v16, v34, v16
	v_mul_f32_e32 v17, v34, v17
	v_mul_f32_e32 v14, v34, v14
	v_mul_f32_e32 v15, v34, v15
	v_mul_f32_e32 v12, v34, v12
	v_mul_f32_e32 v13, v34, v13
	v_mul_f32_e32 v10, v34, v10
	v_mul_f32_e32 v11, v34, v11
	v_mul_f32_e32 v8, v34, v8
	v_mul_f32_e32 v9, v34, v9
	v_mul_f32_e32 v6, v34, v6
	v_mul_f32_e32 v7, v34, v7
	v_mul_f32_e32 v4, v34, v4
	v_mul_f32_e32 v5, v34, v5
	v_mul_f32_e32 v2, v34, v2
	v_mul_f32_e32 v3, v34, v3
	v_cvt_pk_f16_f32 v37, v37, v39
	v_cvt_pk_f16_f32 v36, v38, v36
	v_cvt_pk_f16_f32 v35, v35, v101
	v_cvt_pk_f16_f32 v34, v99, v100
	v_cvt_pk_f16_f32 v41, v47, v48
	v_cvt_pk_f16_f32 v40, v40, v46
	v_cvt_pk_f16_f32 v39, v44, v45
	v_cvt_pk_f16_f32 v38, v42, v43
	s_setprio 1
	s_waitcnt vmcnt(3)
	v_mfma_f32_32x32x16_f16 v[18:33], v[94:97], v[34:37], v[18:33]
	s_waitcnt vmcnt(1)
	v_mfma_f32_32x32x16_f16 v[2:17], v[86:89], v[34:37], v[2:17]
	v_mfma_f32_32x32x16_f16 v[18:33], v[90:93], v[38:41], v[18:33]
	s_waitcnt vmcnt(0)
	v_mfma_f32_32x32x16_f16 v[2:17], v[82:85], v[38:41], v[2:17]
	s_setprio 0
	s_add_i32 s46, s46, 1
	s_add_u32 s2, s2, 0x1000
	s_addc_u32 s3, s3, 0
	s_add_i32 s50, s45, s2
	s_cmp_lg_u32 s50, 0
	s_cbranch_scc0 .LBB2_19
	v_mov_b64_e32 v[100:101], v[68:69]
	v_mov_b64_e32 v[104:105], v[72:73]
	v_mov_b64_e32 v[108:109], v[76:77]
	v_mov_b64_e32 v[34:35], v[78:79]
	v_mov_b32_e32 v115, v135
	v_mov_b32_e32 v131, v134
	v_mov_b64_e32 v[98:99], v[66:67]
	v_mov_b64_e32 v[102:103], v[70:71]
	v_mov_b64_e32 v[106:107], v[74:75]
	v_mov_b64_e32 v[36:37], v[80:81]
	s_branch .LBB2_13
